# layer 1: blocks >= 128 run the 4th MoE weight-absmax item in their idle w_in slot; phase-7 absmax pass then does 3 items per wave
# baseline (speedup 1.0000x reference)
; __device__ __forceinline__ int fresh_tid(int wave) { return wave * 64 + fresh_lane(); }
; __device__ __forceinline__ unsigned xb_ld(unsigned* p)              { return __hip_atomic_load(p, __ATOMIC_RELAXED, __HIP_MEMORY_SCOPE_AGENT); }
; __device__ __forceinline__ unsigned xb_add(unsigned* p, unsigned v) { return __hip_atomic_fetch_add(p, v, __ATOMIC_RELAXED, __HIP_MEMORY_SCOPE_AGENT); }
; __device__ __forceinline__ unsigned xb_xcc_id() { return (unsigned)__builtin_amdgcn_s_getreg((3 << 11) | 20) & 0xFu; }
; #define XB_SPIN(cond, bar) do { unsigned _sp = 0; while (cond) { __builtin_amdgcn_s_sleep(1); \
;     if ((++_sp & 255u) == 0u) { if (xb_ld(&(bar)[XB_TMO])) break; if (_sp > XB_SPIN_CAP) { atomicAdd(&(bar)[XB_TMO], 1u); break; } } } } while (0)
; __device__ __forceinline__ void xcd_barrier(const XcdBarrier& b) {
;     asm volatile("s_waitcnt vmcnt(0)" ::: "memory");
;     __syncthreads();
;     if (fresh_tid(b.wave) == 0) {
;         unsigned* bar = b.bar; asm volatile("" : "+s"(bar));
;         __builtin_amdgcn_s_waitcnt(0);
;         const unsigned bx = xb_xcc_id();
;         unsigned nloc = b.st[0], nx = b.st[1];
;         if (nloc == 0u) { xcd_barrier_complete(bar, bx, nloc, nx); b.st[0] = nloc; b.st[1] = nx; }
;         const unsigned old = xb_add(&bar[XB_XSUB(bx)], 1u);
;         const unsigned gen = old / nloc;
;         if (old + 1u == (gen + 1u) * nloc) {
;             __builtin_amdgcn_fence(__ATOMIC_RELEASE, "agent");
;             asm volatile("s_waitcnt vmcnt(0)" ::: "memory");
;             const unsigned og = xb_add(&bar[XB_TOP], 1u);
;             const unsigned tg = og / nx;
;             if (og + 1u == (tg + 1u) * nx) xb_add(&bar[XB_TOPGEN], 1u);
;             else XB_SPIN(xb_ld(&bar[XB_TOPGEN]) == tg, bar);
;             __builtin_amdgcn_fence(__ATOMIC_ACQUIRE, "agent");
;             xb_add(&bar[XB_XGEN(bx)], 1u);
.LBB0_462:
	s_cmp_lg_u32 s34, 0
	s_cbranch_scc1 .Lepa_skip
	s_cmpk_lg_i32 s78, 0x100
	s_cbranch_scc1 .Lepa_skip
	v_readlane_b32 s4, v253, 0
	s_nop 3
	s_cmpk_lt_u32 s4, 0x80
	s_cbranch_scc1 .Lepa_skip
	s_branch .Lepa_tramp1
.Lepa_ret:
.Lepa_skip:
	s_mov_b32 s0, s93
	s_waitcnt vmcnt(0)
	s_waitcnt lgkmcnt(0)
	s_barrier
	s_nop 0
	v_mbcnt_lo_u32_b32 v0, -1, s0
	v_mbcnt_hi_u32_b32 v0, -1, v0
	v_readlane_b32 s0, v254, 17
	s_nop 1
	v_cmp_eq_u32_e32 vcc, s0, v0
	s_and_saveexec_b64 s[0:1], vcc
	s_cbranch_execz .LBB0_506
	s_bitcmp1_b32 s100, 0
	s_cbranch_scc0 .Lgb2_orig
	v_readlane_b32 s36, v253, 53
	v_readlane_b32 s37, v253, 54
	s_getreg_b32 s2, hwreg(HW_REG_XCC_ID, 0, 4)
	v_mov_b32_e32 v1, 1
	s_and_b32 s2, s2, 15
	s_lshl_b32 s2, s2, 8
	s_addk_i32 s2, 0x1400
	v_mov_b32_e32 v0, s2
	s_waitcnt vmcnt(0) lgkmcnt(0)
	global_atomic_add v2, v0, v1, s[36:37] sc0
	s_waitcnt vmcnt(0)
	v_readfirstlane_b32 s2, v2
	s_lshr_b32 s3, s2, 5
	s_and_b32 s2, s2, 31
	s_add_i32 s3, s3, 1
	s_lshl_b32 s3, s3, 3
	s_cmp_lg_u32 s2, 31
	s_cbranch_scc1 .Lgb2_poll
	buffer_wbl2 sc1
	s_waitcnt vmcnt(0)
	v_add_u32_e32 v0, 0x1000, v0
	global_atomic_add v0, v1, s[36:37]
	v_mov_b32_e32 v0, 0x3400
	global_atomic_add v2, v0, v1, s[36:37] sc0
	s_waitcnt vmcnt(0)
	v_readfirstlane_b32 s2, v2
	s_add_i32 s2, s2, 1
	s_cmp_lg_u32 s2, s3
	s_cbranch_scc1 .Lgb2_poll
	v_mov_b32_e32 v0, 0x3500
	global_atomic_add v0, v1, s[36:37]
	s_branch .Lgb2_done

; #define PG8_BAR __builtin_amdgcn_s_barrier()
; template <class Epi, class Sched, bool ALIGN_EPI = true, bool SP2 = true, bool I8 = false, bool F8 = false>
; __device__ __forceinline__ void gemm_phase(LAS unsigned char* lds, const int K, const Sched& S, const Epi& E, const int wave) {
;     ...
;         if constexpr (ALIGN_EPI) { if (wr == 0) PG8_BAR; }
;         { const int ln_ = fresh_lane();
;           E(acc, cur, wr, wc, ln_ & 15, ln_ >> 4); }
;         if (!has_next) break;
;         if (!(Epi::KEEPS && cur.sub < 2)) {
; #pragma unroll
;         for (int a = 0; a < 2; ++a)
; #pragma unroll
;             for (int b = 0; b < 2; ++b)
; #pragma unroll
;                 for (int m = 0; m < 4; ++m)
; #pragma unroll
;                     for (int n = 0; n < 2; ++n) acc[a][b][m][n] = (acc_t){0, 0, 0, 0};
;         }
;         cur = nxt; cA = nA; cB = nB; ++ui;
;         if constexpr (ALIGN_EPI) { if (wr == 1) PG8_BAR; }
.LBB0_1020:
	s_andn2_b64 vcc, exec, s[2:3]
	s_cbranch_vccnz .LBB0_957
	s_barrier
	s_branch .LBB0_957
.Lepa_tramp1:
	s_branch .Lepa_entry
.Lepa_tramp2:
	s_branch .Lepa_ret
.LBB0_1022:
	s_waitcnt vmcnt(0)
	s_barrier

; __device__ __forceinline__ void phase_moe_weights_a(const Frame& F, const Params& P, int mi, bool dry) {
;     const int gw = F.bid * NWAVES + F.wave, NGW = F.G * NWAVES, lane = F.lane; constexpr int I_A = 2 * (DFF / 64) * 4;
;     for (int it = gw; it < NE * (I_A + I_W2A); it += NGW) { const int e = it / (I_A + I_W2A), r = it - e * (I_A + I_W2A); const size_t eo = ((size_t)mi * NE + e) * D * DFF;
.Lepa_entry:
	s_bitset1_b32 s100, 13
	v_readlane_b32 s38, v253, 1
	v_readlane_b32 s39, v253, 2
	s_mov_b32 s0, 0
	v_mbcnt_lo_u32_b32 v85, -1, 0
	v_mbcnt_hi_u32_b32 v85, -1, v85
	s_nop 0
	v_lshlrev_b32_e32 v112, 2, v85
	s_branch .Lepa_pre

; __device__ __forceinline__ void phase_moe_weights_a(const Frame& F, const Params& P, int mi, bool dry) {
;     const int gw = F.bid * NWAVES + F.wave, NGW = F.G * NWAVES, lane = F.lane; constexpr int I_A = 2 * (DFF / 64) * 4;
;     for (int it = gw; it < NE * (I_A + I_W2A); it += NGW) { const int e = it / (I_A + I_W2A), r = it - e * (I_A + I_W2A); const size_t eo = ((size_t)mi * NE + e) * D * DFF;
;         if (r < I_A) w13_absmax_item(P.in[28] + eo, P.in[29] + eo, P.in[23] + 1 * D, (unsigned*)(F.ws + CTL_AMAX) + (1 + e) * 2 * DFF, r, lane, dry);
;         else w2_absmax_item(P.in[30] + eo, (unsigned*)(F.ws + CTL_AMAX) + AMAX_W2 + 1 + e, r - I_A, lane, dry); }
.Lepa_pre:
	s_movk_i32 s32, 0x1c00
	s_cmpk_eq_i32 s78, 0x100
	s_cselect_b32 s32, 0x1800, s32
	s_add_u32 s1, s38, 0x2ca804
	s_addc_u32 s16, s39, 0
	s_add_u32 s17, s38, 0x280000
	v_readlane_b32 s44, v253, 56
	s_addc_u32 s18, s39, 0
	s_mul_i32 s20, s0, 0x7000000
	v_readlane_b32 s56, v254, 4
	s_mul_hi_i32 s19, s0, 0x7000000
	v_readlane_b32 s57, v254, 5
	s_add_u32 s6, s56, s20
	s_addc_u32 s7, s57, s19
	v_lshl_add_u64 v[0:1], s[6:7], 0, v[112:113]
	v_readlane_b32 s6, v255, 0
	v_cmp_eq_u32_e64 s[4:5], 0, v85
	v_readlane_b32 s21, v254, 43
	v_readlane_b32 s22, v254, 52
	v_readlane_b32 s23, v254, 50
	s_mov_b32 s24, s6
	v_readlane_b32 s28, v254, 25
	v_readlane_b32 s45, v253, 57
	v_readlane_b32 s46, v253, 58
	v_readlane_b32 s47, v253, 59
	v_readlane_b32 s48, v253, 60
	v_readlane_b32 s49, v253, 61
	v_readlane_b32 s50, v253, 62
	v_readlane_b32 s51, v253, 63
	v_readlane_b32 s52, v254, 0
	v_readlane_b32 s53, v254, 1
	v_readlane_b32 s54, v254, 2
	v_readlane_b32 s55, v254, 3
	v_readlane_b32 s58, v254, 6
	v_readlane_b32 s59, v254, 7
	v_readlane_b32 s7, v255, 1
	s_bitcmp1_b32 s100, 13
	s_cbranch_scc0 .Lepa_norm
	s_addk_i32 s24, 0x1400
	s_add_i32 s21, s21, 0x140000
	s_add_i32 s22, s22, 0x50000
	s_add_i32 s23, s23, 0xa000

; __device__ __forceinline__ void phase_moe_weights_a(const Frame& F, const Params& P, int mi, bool dry) {
;     ...
;     for (int it = gw; it < NE * (I_A + I_W2A); it += NGW) { const int e = it / (I_A + I_W2A), r = it - e * (I_A + I_W2A); const size_t eo = ((size_t)mi * NE + e) * D * DFF;
.LBB0_1389:
	s_or_b64 exec, exec, s[6:7]
	v_readlane_b32 s6, v254, 51
	s_add_i32 s24, s24, s76
	s_add_i32 s23, s23, s6
	s_add_i32 s22, s22, s28
	s_add_i32 s21, s21, s89
	s_cmp_lt_i32 s24, s32
	s_cbranch_scc0 .LBB0_1402

; __device__ __forceinline__ void phase_moe_weights_a(const Frame& F, const Params& P, int mi, bool dry) {
;     ...
;     for (int it = gw; it < NE * (I_A + I_W2A); it += NGW) { const int e = it / (I_A + I_W2A), r = it - e * (I_A + I_W2A); const size_t eo = ((size_t)mi * NE + e) * D * DFF;
;         if (r < I_A) w13_absmax_item(P.in[28] + eo, P.in[29] + eo, P.in[23] + 1 * D, (unsigned*)(F.ws + CTL_AMAX) + (1 + e) * 2 * DFF, r, lane, dry);
;         else w2_absmax_item(P.in[30] + eo, (unsigned*)(F.ws + CTL_AMAX) + AMAX_W2 + 1 + e, r - I_A, lane, dry); }
.LBB0_1402:
	s_bitcmp1_b32 s100, 13
	s_cbranch_scc0 .Lepa_cont
	s_bitset0_b32 s100, 13
	s_branch .Lepa_tramp2
